# phase-1 LN1 row loop: the eight norm-gain loads issued with the row's x loads (was one dependent round trip per 256-column piece); plus GEMM2 epilogue, router, combine, diff-combine load batching
# baseline (speedup 1.0000x reference)
; __device__ __forceinline__ unsigned pk2(float lo, float hi) { unsigned r; asm volatile("v_cvt_pk_bf16_f32 %0, %1, %2" : "=v"(r) : "v"(lo), "v"(hi)); return r; }
; __device__ __forceinline__ void stx4(bf16_t* q, const f32x4 v) { u32x2 w; w.x = pk2(v.x, v.y); w.y = pk2(v.z, v.w); *(u32x2*)q = w; }
; #define LAS __attribute__((address_space(3)))
; __device__ __forceinline__ void ph_ln1_first(const P& p, LAS float* ml, int tid, int gw, int nw, int lane) {
;     ...
;   for (int r = gw; r < NTOK; r += nw) {
;     const f32x4* xr = (const f32x4*)(r < CTXL ? p.ctx + (size_t)r * DM : p.x + (size_t)(r - CTXL) * DM);
;     const LAS float* md = ml + (r < CTXL ? 4096 : 0);
;     f32x4 v[8]; float ss = 0;
; #pragma unroll
;     for (int j = 0; j < 8; ++j) { v[j] = __builtin_nontemporal_load(xr + lane + 64 * j); ss += v[j].x * v[j].x + v[j].y * v[j].y + v[j].z * v[j].z + v[j].w * v[j].w; }
;     const float rs = rsqrtf(wave_sum(ss) * (1.f / DM) + EPS);
;     bf16_t* o = WSP(bf16_t, WS_HN) + (size_t)r * DM; bf16_t* xo = WSP(bf16_t, WS_X) + (size_t)r * DM;
; #pragma unroll
;     for (int j = 0; j < 8; ++j) { const int c = (lane + 64 * j) * 4; stx4(xo + c, v[j]);
;       const f32x4 gg = *(const f32x4*)(p.n1 + c), sh = *(const LAS f32x4*)(md + c), sc = *(const LAS f32x4*)(md + DM + c);
;       u32x2 w2; w2.x = pk2(v[j].x * rs * gg.x * (1.f + sc.x) + sh.x, v[j].y * rs * gg.y * (1.f + sc.y) + sh.y); w2.y = pk2(v[j].z * rs * gg.z * (1.f + sc.z) + sh.z, v[j].w * rs * gg.w * (1.f + sc.w) + sh.w);
;       *(u32x2*)(o + c) = w2; }
;   }
.LBB0_99:
	v_lshl_add_u64 v[0:1], v[32:33], 4, v[0:1]
	global_load_dwordx4 v[28:31], v[0:1], off nt
	global_load_dwordx4 v[24:27], v[0:1], off offset:1024 nt
	global_load_dwordx4 v[20:23], v[0:1], off offset:2048 nt
	global_load_dwordx4 v[16:19], v[0:1], off offset:3072 nt
	v_add_co_u32_e32 v54, vcc, s26, v0
	s_lshl_b64 s[22:23], s[22:23], 12
	s_nop 0
	v_addc_co_u32_e32 v55, vcc, 0, v1, vcc
	global_load_dwordx4 v[12:15], v[54:55], off nt
	global_load_dwordx4 v[8:11], v[54:55], off offset:1024 nt
	global_load_dwordx4 v[4:7], v[54:55], off offset:2048 nt
	global_load_dwordx4 v[0:3], v[54:55], off offset:3072 nt
	v_lshl_add_u64 v[54:55], v[46:47], 0, s[22:23]
	v_lshl_add_u32 v72, s28, 2, v35
	s_add_u32 s20, s20, s24
	s_addc_u32 s21, s21, s25
	s_cmpk_lt_i32 s20, 0x2100
	v_lshl_add_u64 v[52:53], v[52:53], 0, v[50:51]
	global_load_dwordx4 v[84:87], v[36:37], off
	global_load_dwordx4 v[88:91], v[36:37], off offset:1024
	global_load_dwordx4 v[92:95], v[36:37], off offset:2048
	global_load_dwordx4 v[96:99], v[36:37], off offset:3072
	global_load_dwordx4 v[100:103], v[38:39], off
	global_load_dwordx4 v[104:107], v[40:41], off
	global_load_dwordx4 v[108:111], v[42:43], off
	global_load_dwordx4 v[112:115], v[44:45], off
	s_waitcnt vmcnt(0)
	v_cvt_pk_bf16_f32 v56, v28, v29
	v_cvt_pk_bf16_f32 v57, v30, v31
	global_store_dwordx2 v[54:55], v[56:57], off
	v_mul_f32_e32 v73, v29, v29
	v_mul_f32_e32 v74, v25, v25
	v_mul_f32_e32 v75, v21, v21
	v_fmac_f32_e32 v73, v28, v28
	v_fmac_f32_e32 v74, v24, v24
	v_mul_f32_e32 v76, v17, v17
	v_fmac_f32_e32 v75, v20, v20
	v_fmac_f32_e32 v73, v30, v30
	v_fmac_f32_e32 v74, v26, v26
	v_fmac_f32_e32 v76, v16, v16
	v_mul_f32_e32 v77, v13, v13
	v_fmac_f32_e32 v75, v22, v22
	v_fmac_f32_e32 v73, v31, v31
	v_fmac_f32_e32 v74, v27, v27
	v_mul_f32_e32 v78, v9, v9
	v_fmac_f32_e32 v76, v18, v18
	v_fmac_f32_e32 v77, v12, v12
	v_fmac_f32_e32 v75, v23, v23
	v_add_f32_e32 v73, v73, v74
	v_mul_f32_e32 v79, v5, v5
	v_fmac_f32_e32 v78, v8, v8
	v_fmac_f32_e32 v76, v19, v19
	v_fmac_f32_e32 v77, v14, v14
	v_add_f32_e32 v73, v73, v75
	v_mul_f32_e32 v80, v1, v1
	v_fmac_f32_e32 v79, v4, v4
	v_fmac_f32_e32 v78, v10, v10
	v_fmac_f32_e32 v77, v15, v15
	v_add_f32_e32 v73, v73, v76
	v_fmac_f32_e32 v80, v0, v0
	v_fmac_f32_e32 v79, v6, v6
	v_fmac_f32_e32 v78, v11, v11
	v_add_f32_e32 v73, v73, v77
	v_fmac_f32_e32 v80, v2, v2
	v_fmac_f32_e32 v79, v7, v7
	v_add_f32_e32 v73, v73, v78
	v_fmac_f32_e32 v80, v3, v3
	v_add_f32_e32 v73, v73, v79
	v_add_f32_e32 v73, v73, v80
	ds_read_b128 v[64:67], v72 offset:8192
	ds_read_b128 v[68:71], v72
	v_add_f32_dpp v73, v73, v73 quad_perm:[1,0,3,2] row_mask:0xf bank_mask:0xf bound_ctrl:1
	v_lshl_add_u64 v[56:57], v[48:49], 0, s[22:23]
	s_waitcnt lgkmcnt(1)
	v_add_f32_e32 v64, 1.0, v64
	v_add_f32_dpp v73, v73, v73 quad_perm:[2,3,0,1] row_mask:0xf bank_mask:0xf bound_ctrl:1
	v_add_f32_e32 v65, 1.0, v65
	v_add_f32_e32 v66, 1.0, v66
	v_add_f32_dpp v73, v73, v73 row_half_mirror row_mask:0xf bank_mask:0xf bound_ctrl:1
	v_add_f32_e32 v67, 1.0, v67
	s_nop 0
	v_add_f32_dpp v73, v73, v73 row_mirror row_mask:0xf bank_mask:0xf bound_ctrl:1
	v_mov_b32_e32 v74, v73
	s_nop 1
	v_permlane16_swap_b32_e32 v73, v74
	v_add_f32_e32 v73, v73, v74
	v_mov_b32_e32 v74, v73
	s_nop 1
	v_permlane32_swap_b32_e32 v73, v74
	v_add_f32_e32 v73, v73, v74
	v_fmamk_f32 v73, v73, 0x3a000000, v59
	v_mul_f32_e32 v74, 0x4b800000, v73
	v_cmp_gt_f32_e32 vcc, s27, v73
	s_nop 1
	v_cndmask_b32_e32 v73, v73, v74, vcc
	v_rsq_f32_e32 v73, v73
	s_nop 0
	v_mul_f32_e32 v74, 0x45800000, v73
	v_cndmask_b32_e32 v73, v73, v74, vcc
	v_mul_f32_e32 v28, v28, v73
	v_mul_f32_e32 v29, v29, v73
	v_mul_f32_e32 v30, v30, v73
	v_mul_f32_e32 v31, v31, v73
	v_mul_f32_e32 v28, v84, v28
	v_mul_f32_e32 v29, v85, v29
	v_mul_f32_e32 v30, v86, v30
	v_mul_f32_e32 v31, v87, v31
	s_waitcnt lgkmcnt(0)
	v_fma_f32 v28, v64, v28, v68
	v_fma_f32 v29, v65, v29, v69
	v_fmac_f32_e32 v71, v67, v31
	v_fma_f32 v30, v66, v30, v70
	v_cvt_pk_bf16_f32 v28, v28, v29
	v_cvt_pk_bf16_f32 v29, v30, v71
	global_store_dwordx2 v[56:57], v[28:29], off
	v_cvt_pk_bf16_f32 v28, v24, v25
	v_cvt_pk_bf16_f32 v29, v26, v27
	global_store_dwordx2 v[54:55], v[28:29], off offset:512
	ds_read_b128 v[60:63], v72 offset:9216
	v_mul_f32_e32 v64, v24, v73
	v_mul_f32_e32 v65, v25, v73
	v_mul_f32_e32 v66, v26, v73
	v_mul_f32_e32 v67, v27, v73
	ds_read_b128 v[24:27], v72 offset:1024
	s_waitcnt lgkmcnt(1)
	v_add_f32_e32 v60, 1.0, v60
	v_add_f32_e32 v61, 1.0, v61
	v_add_f32_e32 v62, 1.0, v62
	v_add_f32_e32 v63, 1.0, v63
	v_mul_f32_e32 v28, v64, v88
	v_mul_f32_e32 v29, v65, v89
	v_mul_f32_e32 v30, v66, v90
	v_mul_f32_e32 v31, v67, v91
	s_waitcnt lgkmcnt(0)
; __device__ __forceinline__ unsigned pk2(float lo, float hi) { unsigned r; asm volatile("v_cvt_pk_bf16_f32 %0, %1, %2" : "=v"(r) : "v"(lo), "v"(hi)); return r; }
; __device__ __forceinline__ void stx4(bf16_t* q, const f32x4 v) { u32x2 w; w.x = pk2(v.x, v.y); w.y = pk2(v.z, v.w); *(u32x2*)q = w; }
; #define LAS __attribute__((address_space(3)))
; __device__ __forceinline__ void ph_ln1_first(const P& p, LAS float* ml, int tid, int gw, int nw, int lane) {
;     ...
;     bf16_t* o = WSP(bf16_t, WS_HN) + (size_t)r * DM; bf16_t* xo = WSP(bf16_t, WS_X) + (size_t)r * DM;
; #pragma unroll
;     for (int j = 0; j < 8; ++j) { const int c = (lane + 64 * j) * 4; stx4(xo + c, v[j]);
;       const f32x4 gg = *(const f32x4*)(p.n1 + c), sh = *(const LAS f32x4*)(md + c), sc = *(const LAS f32x4*)(md + DM + c);
;       u32x2 w2; w2.x = pk2(v[j].x * rs * gg.x * (1.f + sc.x) + sh.x, v[j].y * rs * gg.y * (1.f + sc.y) + sh.y); w2.y = pk2(v[j].z * rs * gg.z * (1.f + sc.z) + sh.z, v[j].w * rs * gg.w * (1.f + sc.w) + sh.w);
;       *(u32x2*)(o + c) = w2; }
;   }
	v_fma_f32 v24, v28, v60, v24
	v_fma_f32 v25, v29, v61, v25
	v_fmac_f32_e32 v27, v31, v63
	v_fma_f32 v26, v30, v62, v26
	v_cvt_pk_bf16_f32 v24, v24, v25
	v_cvt_pk_bf16_f32 v25, v26, v27
	global_store_dwordx2 v[56:57], v[24:25], off offset:512
	v_cvt_pk_bf16_f32 v24, v20, v21
	v_cvt_pk_bf16_f32 v25, v22, v23
	global_store_dwordx2 v[54:55], v[24:25], off offset:1024
	ds_read_b128 v[28:31], v72 offset:10240
	v_mul_f32_e32 v60, v20, v73
	v_mul_f32_e32 v61, v21, v73
	v_mul_f32_e32 v62, v22, v73
	v_mul_f32_e32 v63, v23, v73
	ds_read_b128 v[20:23], v72 offset:2048
	s_waitcnt lgkmcnt(1)
	v_add_f32_e32 v28, 1.0, v28
	v_add_f32_e32 v29, 1.0, v29
	v_add_f32_e32 v30, 1.0, v30
	v_add_f32_e32 v31, 1.0, v31
	v_mul_f32_e32 v24, v60, v92
	v_mul_f32_e32 v25, v61, v93
	v_mul_f32_e32 v26, v62, v94
	v_mul_f32_e32 v27, v63, v95
	s_waitcnt lgkmcnt(0)
	v_fma_f32 v20, v24, v28, v20
	v_fma_f32 v21, v25, v29, v21
	v_fma_f32 v22, v26, v30, v22
	v_fmac_f32_e32 v23, v27, v31
	v_cvt_pk_bf16_f32 v20, v20, v21
	v_cvt_pk_bf16_f32 v21, v22, v23
	global_store_dwordx2 v[56:57], v[20:21], off offset:1024
	v_cvt_pk_bf16_f32 v20, v16, v17
	v_cvt_pk_bf16_f32 v21, v18, v19
	global_store_dwordx2 v[54:55], v[20:21], off offset:1536
	ds_read_b128 v[24:27], v72 offset:11264
	v_mul_f32_e32 v28, v16, v73
	v_mul_f32_e32 v29, v17, v73
	v_mul_f32_e32 v30, v18, v73
	v_mul_f32_e32 v31, v19, v73
	ds_read_b128 v[16:19], v72 offset:3072
	s_waitcnt lgkmcnt(1)
	v_add_f32_e32 v24, 1.0, v24
	v_add_f32_e32 v25, 1.0, v25
	v_add_f32_e32 v26, 1.0, v26
	v_add_f32_e32 v27, 1.0, v27
	v_mul_f32_e32 v20, v28, v96
	v_mul_f32_e32 v21, v29, v97
	v_mul_f32_e32 v22, v30, v98
	v_mul_f32_e32 v23, v31, v99
	s_waitcnt lgkmcnt(0)
	v_fma_f32 v16, v20, v24, v16
	v_fma_f32 v17, v21, v25, v17
	v_fma_f32 v18, v22, v26, v18
	v_fmac_f32_e32 v19, v23, v27
	v_cvt_pk_bf16_f32 v16, v16, v17
	v_cvt_pk_bf16_f32 v17, v18, v19
	global_store_dwordx2 v[56:57], v[16:17], off offset:1536
	v_cvt_pk_bf16_f32 v16, v12, v13
	v_cvt_pk_bf16_f32 v17, v14, v15
	global_store_dwordx2 v[54:55], v[16:17], off offset:2048
	ds_read_b128 v[20:23], v72 offset:4096
	ds_read_b128 v[24:27], v72 offset:12288
	v_mul_f32_e32 v12, v12, v73
	v_mul_f32_e32 v13, v13, v73
	v_mul_f32_e32 v14, v14, v73
	v_mul_f32_e32 v15, v15, v73
	s_waitcnt lgkmcnt(0)
	v_add_f32_e32 v24, 1.0, v24
	v_add_f32_e32 v25, 1.0, v25
	v_add_f32_e32 v26, 1.0, v26
	v_add_f32_e32 v27, 1.0, v27
	v_mul_f32_e32 v12, v12, v100
	v_mul_f32_e32 v13, v13, v101
	v_mul_f32_e32 v14, v14, v102
	v_mul_f32_e32 v15, v15, v103
	v_fma_f32 v12, v12, v24, v20
	v_fma_f32 v13, v13, v25, v21
	v_fma_f32 v14, v14, v26, v22
	v_fmac_f32_e32 v23, v15, v27
	v_cvt_pk_bf16_f32 v12, v12, v13
	v_cvt_pk_bf16_f32 v13, v14, v23
	global_store_dwordx2 v[56:57], v[12:13], off offset:2048
	v_cvt_pk_bf16_f32 v12, v8, v9
	v_cvt_pk_bf16_f32 v13, v10, v11
	global_store_dwordx2 v[54:55], v[12:13], off offset:2560
	ds_read_b128 v[16:19], v72 offset:5120
	ds_read_b128 v[20:23], v72 offset:13312
	v_mul_f32_e32 v8, v8, v73
	v_mul_f32_e32 v9, v9, v73
	v_mul_f32_e32 v10, v10, v73
	v_mul_f32_e32 v11, v11, v73
	s_waitcnt lgkmcnt(0)
	v_add_f32_e32 v20, 1.0, v20
	v_add_f32_e32 v21, 1.0, v21
	v_add_f32_e32 v22, 1.0, v22
	v_add_f32_e32 v23, 1.0, v23
	v_mul_f32_e32 v8, v8, v104
	v_mul_f32_e32 v9, v9, v105
	v_mul_f32_e32 v10, v10, v106
	v_mul_f32_e32 v11, v11, v107
	v_fma_f32 v8, v8, v20, v16
	v_fma_f32 v9, v9, v21, v17
	v_fma_f32 v10, v10, v22, v18
	v_fmac_f32_e32 v19, v11, v23
	v_cvt_pk_bf16_f32 v8, v8, v9
	v_cvt_pk_bf16_f32 v9, v10, v19
	global_store_dwordx2 v[56:57], v[8:9], off offset:2560
	v_cvt_pk_bf16_f32 v8, v4, v5
	v_cvt_pk_bf16_f32 v9, v6, v7
	global_store_dwordx2 v[54:55], v[8:9], off offset:3072
	ds_read_b128 v[12:15], v72 offset:6144
	ds_read_b128 v[16:19], v72 offset:14336
	v_mul_f32_e32 v4, v4, v73
	v_mul_f32_e32 v5, v5, v73
	v_mul_f32_e32 v6, v6, v73
	v_mul_f32_e32 v7, v7, v73
	s_waitcnt lgkmcnt(0)
	v_add_f32_e32 v16, 1.0, v16
	v_add_f32_e32 v17, 1.0, v17
	v_add_f32_e32 v18, 1.0, v18
	v_add_f32_e32 v19, 1.0, v19
	v_mul_f32_e32 v4, v4, v108
	v_mul_f32_e32 v5, v5, v109
	v_mul_f32_e32 v6, v6, v110
	v_mul_f32_e32 v7, v7, v111
	v_fma_f32 v4, v4, v16, v12
	v_fma_f32 v5, v5, v17, v13
	v_fma_f32 v6, v6, v18, v14
	v_fmac_f32_e32 v15, v7, v19
	v_cvt_pk_bf16_f32 v4, v4, v5
	v_cvt_pk_bf16_f32 v5, v6, v15
	global_store_dwordx2 v[56:57], v[4:5], off offset:3072
	v_cvt_pk_bf16_f32 v4, v0, v1
	v_cvt_pk_bf16_f32 v5, v2, v3
	global_store_dwordx2 v[54:55], v[4:5], off offset:3584
	ds_read_b128 v[8:11], v72 offset:7168
	ds_read_b128 v[12:15], v72 offset:15360
	v_mul_f32_e32 v0, v0, v73
	v_mul_f32_e32 v1, v1, v73
	v_mul_f32_e32 v2, v2, v73
	v_mul_f32_e32 v3, v3, v73
	s_waitcnt lgkmcnt(0)
	v_add_f32_e32 v12, 1.0, v12
	v_add_f32_e32 v13, 1.0, v13
	v_add_f32_e32 v14, 1.0, v14
	v_add_f32_e32 v15, 1.0, v15
	v_mul_f32_e32 v0, v0, v112
	v_mul_f32_e32 v1, v1, v113
	v_mul_f32_e32 v2, v2, v114
	v_mul_f32_e32 v3, v3, v115
	v_fma_f32 v0, v0, v12, v8
	v_fma_f32 v1, v1, v13, v9
	v_fma_f32 v2, v2, v14, v10
	v_fmac_f32_e32 v11, v3, v15
	v_cvt_pk_bf16_f32 v0, v0, v1
	v_cvt_pk_bf16_f32 v1, v2, v11
	global_store_dwordx2 v[56:57], v[0:1], off offset:3584
	s_cbranch_scc0 .LBB0_102
